# v31 + slow-path candidate loop reuses the prefetched screening-argmin row
# baseline (speedup 1.0000x reference)
.LBB0_138:
	s_ff1_i32_b64 s19, s[26:27]
	s_add_u32 s30, s26, -1
	s_addc_u32 s31, s27, -1
	s_lshl_b32 s24, s19, 10
	v_lshl_add_u64 v[16:17], v[2:3], 0, s[24:25]
	s_cmp_lg_u32 s19, s92
	s_cbranch_scc1 .Lsp_miss0
	s_waitcnt vmcnt(0)
	v_mov_b64_e32 v[20:21], v[70:71]
	v_mov_b64_e32 v[22:23], v[72:73]
	s_branch .Lsp_join0
.Lsp_miss0:
	global_load_dwordx4 v[20:23], v[16:17], off
.Lsp_join0:
	s_and_b64 s[26:27], s[30:31], s[26:27]
	s_waitcnt vmcnt(0)
	v_cvt_f64_f32_e32 v[16:17], v20
	v_cvt_f64_f32_e32 v[20:21], v21
	v_mul_f64 v[26:27], v[6:7], v[20:21]
	v_mul_f64 v[20:21], v[20:21], v[20:21]
	v_cvt_f64_f32_e32 v[24:25], v22
	v_fmac_f64_e32 v[26:27], v[4:5], v[16:17]
	v_fmac_f64_e32 v[20:21], v[16:17], v[16:17]
	v_cvt_f64_f32_e32 v[22:23], v23
	v_fmac_f64_e32 v[26:27], v[8:9], v[24:25]
	v_fmac_f64_e32 v[20:21], v[24:25], v[24:25]
	v_fmac_f64_e32 v[26:27], v[10:11], v[22:23]
	v_fmac_f64_e32 v[20:21], v[22:23], v[22:23]
	s_nop 0
	v_mov_b32_dpp v16, v26 quad_perm:[1,0,3,2] row_mask:0xf bank_mask:0xf bound_ctrl:1
	v_mov_b32_dpp v17, v27 quad_perm:[1,0,3,2] row_mask:0xf bank_mask:0xf bound_ctrl:1
	v_mov_b32_dpp v22, v20 quad_perm:[1,0,3,2] row_mask:0xf bank_mask:0xf bound_ctrl:1
	v_mov_b32_dpp v23, v21 quad_perm:[1,0,3,2] row_mask:0xf bank_mask:0xf bound_ctrl:1
	v_add_f64 v[16:17], v[26:27], v[16:17]
	v_add_f64 v[20:21], v[20:21], v[22:23]
	s_nop 0
	v_mov_b32_dpp v22, v16 quad_perm:[2,3,0,1] row_mask:0xf bank_mask:0xf bound_ctrl:1
	v_mov_b32_dpp v23, v17 quad_perm:[2,3,0,1] row_mask:0xf bank_mask:0xf bound_ctrl:1
	v_mov_b32_dpp v24, v20 quad_perm:[2,3,0,1] row_mask:0xf bank_mask:0xf bound_ctrl:1
	v_mov_b32_dpp v25, v21 quad_perm:[2,3,0,1] row_mask:0xf bank_mask:0xf bound_ctrl:1
	v_add_f64 v[16:17], v[16:17], v[22:23]
	v_add_f64 v[20:21], v[20:21], v[24:25]
	s_nop 0
	v_mov_b32_dpp v22, v16 row_half_mirror row_mask:0xf bank_mask:0xf bound_ctrl:1
	v_mov_b32_dpp v23, v17 row_half_mirror row_mask:0xf bank_mask:0xf bound_ctrl:1
	v_mov_b32_dpp v24, v20 row_half_mirror row_mask:0xf bank_mask:0xf bound_ctrl:1
	v_mov_b32_dpp v25, v21 row_half_mirror row_mask:0xf bank_mask:0xf bound_ctrl:1
	v_add_f64 v[16:17], v[16:17], v[22:23]
	v_add_f64 v[20:21], v[20:21], v[24:25]
	s_nop 0
	v_mov_b32_dpp v22, v16 row_mirror row_mask:0xf bank_mask:0xf bound_ctrl:1
	v_mov_b32_dpp v23, v17 row_mirror row_mask:0xf bank_mask:0xf bound_ctrl:1
	v_mov_b32_dpp v24, v20 row_mirror row_mask:0xf bank_mask:0xf bound_ctrl:1
	v_mov_b32_dpp v25, v21 row_mirror row_mask:0xf bank_mask:0xf bound_ctrl:1
	v_add_f64 v[16:17], v[16:17], v[22:23]
	v_add_f64 v[20:21], v[20:21], v[24:25]
	v_readlane_b32 s23, v17, 16
	v_readlane_b32 s24, v16, 16
	v_readlane_b32 s33, v17, 48
	v_readlane_b32 s40, v16, 48
	v_readlane_b32 s41, v21, 16
	v_readlane_b32 s42, v20, 16
	v_readlane_b32 s43, v21, 48
	v_readlane_b32 s44, v20, 48
	v_readlane_b32 s31, v17, 0
	v_readlane_b32 s30, v16, 0
	v_readlane_b32 s35, v17, 32
	v_readlane_b32 s34, v16, 32
	v_readlane_b32 s37, v21, 0
	v_readlane_b32 s36, v20, 0
	v_readlane_b32 s39, v21, 32
	v_readlane_b32 s38, v20, 32
	v_mov_b32_e32 v16, s24
	v_mov_b32_e32 v17, s23
	v_mov_b32_e32 v20, s40
	v_mov_b32_e32 v21, s33
	v_mov_b32_e32 v22, s42
	v_mov_b32_e32 v23, s41
	v_mov_b32_e32 v24, s44
	v_mov_b32_e32 v25, s43
	v_add_f64 v[16:17], s[30:31], v[16:17]
	v_add_f64 v[20:21], s[34:35], v[20:21]
	v_add_f64 v[22:23], s[36:37], v[22:23]
	v_add_f64 v[24:25], s[38:39], v[24:25]
	v_add_f64 v[16:17], v[16:17], v[20:21]
	v_add_f64 v[20:21], v[22:23], v[24:25]
	v_add_f64 v[20:21], v[12:13], v[20:21]
	v_fmac_f64_e32 v[20:21], -2.0, v[16:17]
	v_cvt_f32_f64_e32 v16, v[20:21]
	v_cmp_gt_f32_e32 vcc, v15, v16
	s_and_b64 s[30:31], vcc, exec
	s_cselect_b32 s22, s19, s22
	v_cndmask_b32_e32 v15, v15, v16, vcc
	s_cmp_lg_u64 s[26:27], 0
	s_cbranch_scc1 .LBB0_138

.LBB0_141:
	s_ff1_i32_b64 s19, s[26:27]
	s_add_u32 s30, s26, -1
	s_addc_u32 s31, s27, -1
	s_lshl_b32 s24, s19, 10
	v_lshl_add_u64 v[16:17], v[2:3], 0, s[24:25]
	s_cmp_lg_u32 s19, s93
	s_cbranch_scc1 .Lsp_miss1
	s_waitcnt vmcnt(0)
	v_mov_b64_e32 v[20:21], v[74:75]
	v_mov_b64_e32 v[22:23], v[76:77]
	s_branch .Lsp_join1

.Lsp_join1:
	s_and_b64 s[26:27], s[30:31], s[26:27]
	s_waitcnt vmcnt(0)
	v_cvt_f64_f32_e32 v[16:17], v20
	v_cvt_f64_f32_e32 v[20:21], v21
	v_mul_f64 v[26:27], v[6:7], v[20:21]
	v_mul_f64 v[20:21], v[20:21], v[20:21]
	v_cvt_f64_f32_e32 v[24:25], v22
	v_fmac_f64_e32 v[26:27], v[4:5], v[16:17]
	v_fmac_f64_e32 v[20:21], v[16:17], v[16:17]
	v_cvt_f64_f32_e32 v[22:23], v23
	v_fmac_f64_e32 v[26:27], v[8:9], v[24:25]
	v_fmac_f64_e32 v[20:21], v[24:25], v[24:25]
	v_fmac_f64_e32 v[26:27], v[10:11], v[22:23]
	v_fmac_f64_e32 v[20:21], v[22:23], v[22:23]
	s_nop 0
	v_mov_b32_dpp v16, v26 quad_perm:[1,0,3,2] row_mask:0xf bank_mask:0xf bound_ctrl:1
	v_mov_b32_dpp v17, v27 quad_perm:[1,0,3,2] row_mask:0xf bank_mask:0xf bound_ctrl:1
	v_mov_b32_dpp v22, v20 quad_perm:[1,0,3,2] row_mask:0xf bank_mask:0xf bound_ctrl:1
	v_mov_b32_dpp v23, v21 quad_perm:[1,0,3,2] row_mask:0xf bank_mask:0xf bound_ctrl:1
	v_add_f64 v[16:17], v[26:27], v[16:17]
	v_add_f64 v[20:21], v[20:21], v[22:23]
	s_nop 0
	v_mov_b32_dpp v22, v16 quad_perm:[2,3,0,1] row_mask:0xf bank_mask:0xf bound_ctrl:1
	v_mov_b32_dpp v23, v17 quad_perm:[2,3,0,1] row_mask:0xf bank_mask:0xf bound_ctrl:1
	v_mov_b32_dpp v24, v20 quad_perm:[2,3,0,1] row_mask:0xf bank_mask:0xf bound_ctrl:1
	v_mov_b32_dpp v25, v21 quad_perm:[2,3,0,1] row_mask:0xf bank_mask:0xf bound_ctrl:1
	v_add_f64 v[16:17], v[16:17], v[22:23]
	v_add_f64 v[20:21], v[20:21], v[24:25]
	s_nop 0
	v_mov_b32_dpp v22, v16 row_half_mirror row_mask:0xf bank_mask:0xf bound_ctrl:1
	v_mov_b32_dpp v23, v17 row_half_mirror row_mask:0xf bank_mask:0xf bound_ctrl:1
	v_mov_b32_dpp v24, v20 row_half_mirror row_mask:0xf bank_mask:0xf bound_ctrl:1
	v_mov_b32_dpp v25, v21 row_half_mirror row_mask:0xf bank_mask:0xf bound_ctrl:1
	v_add_f64 v[16:17], v[16:17], v[22:23]
	v_add_f64 v[20:21], v[20:21], v[24:25]
	s_nop 0
	v_mov_b32_dpp v22, v16 row_mirror row_mask:0xf bank_mask:0xf bound_ctrl:1
	v_mov_b32_dpp v23, v17 row_mirror row_mask:0xf bank_mask:0xf bound_ctrl:1
	v_mov_b32_dpp v24, v20 row_mirror row_mask:0xf bank_mask:0xf bound_ctrl:1
	v_mov_b32_dpp v25, v21 row_mirror row_mask:0xf bank_mask:0xf bound_ctrl:1
	v_add_f64 v[16:17], v[16:17], v[22:23]
	v_add_f64 v[20:21], v[20:21], v[24:25]
	v_readlane_b32 s23, v17, 16
	v_readlane_b32 s24, v16, 16
	v_readlane_b32 s33, v17, 48
	v_readlane_b32 s40, v16, 48
	v_readlane_b32 s41, v21, 16
	v_readlane_b32 s42, v20, 16
	v_readlane_b32 s43, v21, 48
	v_readlane_b32 s44, v20, 48
	v_readlane_b32 s31, v17, 0
	v_readlane_b32 s30, v16, 0
	v_readlane_b32 s35, v17, 32
	v_readlane_b32 s34, v16, 32
	v_readlane_b32 s37, v21, 0
	v_readlane_b32 s36, v20, 0
	v_readlane_b32 s39, v21, 32
	v_readlane_b32 s38, v20, 32
	v_mov_b32_e32 v16, s24
	v_mov_b32_e32 v17, s23
	v_mov_b32_e32 v20, s40
	v_mov_b32_e32 v21, s33
	v_mov_b32_e32 v22, s42
	v_mov_b32_e32 v23, s41
	v_mov_b32_e32 v24, s44
	v_mov_b32_e32 v25, s43
	v_add_f64 v[16:17], s[30:31], v[16:17]
	v_add_f64 v[20:21], s[34:35], v[20:21]
	v_add_f64 v[22:23], s[36:37], v[22:23]
	v_add_f64 v[24:25], s[38:39], v[24:25]
	v_add_f64 v[16:17], v[16:17], v[20:21]
	v_add_f64 v[20:21], v[22:23], v[24:25]
	v_add_f64 v[20:21], v[12:13], v[20:21]
	v_fmac_f64_e32 v[20:21], -2.0, v[16:17]
	v_cvt_f32_f64_e32 v16, v[20:21]
	v_cmp_gt_f32_e32 vcc, v15, v16
	s_and_b64 s[30:31], vcc, exec
	s_cselect_b32 s8, s19, s8
	v_cndmask_b32_e32 v15, v15, v16, vcc
	s_cmp_lg_u64 s[26:27], 0
	s_cbranch_scc1 .LBB0_141

.LBB0_144:
	s_ff1_i32_b64 s6, s[26:27]
	s_add_u32 s30, s26, -1
	s_addc_u32 s31, s27, -1
	s_lshl_b32 s24, s6, 10
	v_lshl_add_u64 v[16:17], v[2:3], 0, s[24:25]
	s_cmp_lg_u32 s6, s94
	s_cbranch_scc1 .Lsp_miss2
	s_waitcnt vmcnt(0)
	v_mov_b64_e32 v[20:21], v[78:79]
	v_mov_b64_e32 v[22:23], v[80:81]
	s_branch .Lsp_join2

.Lsp_join2:
	s_and_b64 s[26:27], s[30:31], s[26:27]
	s_waitcnt vmcnt(0)
	v_cvt_f64_f32_e32 v[16:17], v20
	v_cvt_f64_f32_e32 v[20:21], v21
	v_mul_f64 v[26:27], v[6:7], v[20:21]
	v_mul_f64 v[20:21], v[20:21], v[20:21]
	v_cvt_f64_f32_e32 v[24:25], v22
	v_fmac_f64_e32 v[26:27], v[4:5], v[16:17]
	v_fmac_f64_e32 v[20:21], v[16:17], v[16:17]
	v_cvt_f64_f32_e32 v[22:23], v23
	v_fmac_f64_e32 v[26:27], v[8:9], v[24:25]
	v_fmac_f64_e32 v[20:21], v[24:25], v[24:25]
	v_fmac_f64_e32 v[26:27], v[10:11], v[22:23]
	v_fmac_f64_e32 v[20:21], v[22:23], v[22:23]
	s_nop 0
	v_mov_b32_dpp v16, v26 quad_perm:[1,0,3,2] row_mask:0xf bank_mask:0xf bound_ctrl:1
	v_mov_b32_dpp v17, v27 quad_perm:[1,0,3,2] row_mask:0xf bank_mask:0xf bound_ctrl:1
	v_mov_b32_dpp v22, v20 quad_perm:[1,0,3,2] row_mask:0xf bank_mask:0xf bound_ctrl:1
	v_mov_b32_dpp v23, v21 quad_perm:[1,0,3,2] row_mask:0xf bank_mask:0xf bound_ctrl:1
	v_add_f64 v[16:17], v[26:27], v[16:17]
	v_add_f64 v[20:21], v[20:21], v[22:23]
	s_nop 0
	v_mov_b32_dpp v22, v16 quad_perm:[2,3,0,1] row_mask:0xf bank_mask:0xf bound_ctrl:1
	v_mov_b32_dpp v23, v17 quad_perm:[2,3,0,1] row_mask:0xf bank_mask:0xf bound_ctrl:1
	v_mov_b32_dpp v24, v20 quad_perm:[2,3,0,1] row_mask:0xf bank_mask:0xf bound_ctrl:1
	v_mov_b32_dpp v25, v21 quad_perm:[2,3,0,1] row_mask:0xf bank_mask:0xf bound_ctrl:1
	v_add_f64 v[16:17], v[16:17], v[22:23]
	v_add_f64 v[20:21], v[20:21], v[24:25]
	s_nop 0
	v_mov_b32_dpp v22, v16 row_half_mirror row_mask:0xf bank_mask:0xf bound_ctrl:1
	v_mov_b32_dpp v23, v17 row_half_mirror row_mask:0xf bank_mask:0xf bound_ctrl:1
	v_mov_b32_dpp v24, v20 row_half_mirror row_mask:0xf bank_mask:0xf bound_ctrl:1
	v_mov_b32_dpp v25, v21 row_half_mirror row_mask:0xf bank_mask:0xf bound_ctrl:1
	v_add_f64 v[16:17], v[16:17], v[22:23]
	v_add_f64 v[20:21], v[20:21], v[24:25]
	s_nop 0
	v_mov_b32_dpp v22, v16 row_mirror row_mask:0xf bank_mask:0xf bound_ctrl:1
	v_mov_b32_dpp v23, v17 row_mirror row_mask:0xf bank_mask:0xf bound_ctrl:1
	v_mov_b32_dpp v24, v20 row_mirror row_mask:0xf bank_mask:0xf bound_ctrl:1
	v_mov_b32_dpp v25, v21 row_mirror row_mask:0xf bank_mask:0xf bound_ctrl:1
	v_add_f64 v[16:17], v[16:17], v[22:23]
	v_add_f64 v[20:21], v[20:21], v[24:25]
	v_readlane_b32 s19, v17, 16
	v_readlane_b32 s23, v16, 16
	v_readlane_b32 s24, v17, 48
	v_readlane_b32 s33, v16, 48
	v_readlane_b32 s40, v21, 16
	v_readlane_b32 s41, v20, 16
	v_readlane_b32 s42, v21, 48
	v_readlane_b32 s43, v20, 48
	v_readlane_b32 s31, v17, 0
	v_readlane_b32 s30, v16, 0
	v_readlane_b32 s35, v17, 32
	v_readlane_b32 s34, v16, 32
	v_readlane_b32 s37, v21, 0
	v_readlane_b32 s36, v20, 0
	v_readlane_b32 s39, v21, 32
	v_readlane_b32 s38, v20, 32
	v_mov_b32_e32 v16, s23
	v_mov_b32_e32 v17, s19
	v_mov_b32_e32 v20, s33
	v_mov_b32_e32 v21, s24
	v_mov_b32_e32 v22, s41
	v_mov_b32_e32 v23, s40
	v_mov_b32_e32 v24, s43
	v_mov_b32_e32 v25, s42
	v_add_f64 v[16:17], s[30:31], v[16:17]
	v_add_f64 v[20:21], s[34:35], v[20:21]
	v_add_f64 v[22:23], s[36:37], v[22:23]
	v_add_f64 v[24:25], s[38:39], v[24:25]
	v_add_f64 v[16:17], v[16:17], v[20:21]
	v_add_f64 v[20:21], v[22:23], v[24:25]
	v_add_f64 v[20:21], v[12:13], v[20:21]
	v_fmac_f64_e32 v[20:21], -2.0, v[16:17]
	v_cvt_f32_f64_e32 v16, v[20:21]
	v_cmp_gt_f32_e32 vcc, v15, v16
	s_and_b64 s[30:31], vcc, exec
	s_cselect_b32 s0, s6, s0
	v_cndmask_b32_e32 v15, v15, v16, vcc
	s_cmp_lg_u64 s[26:27], 0
	s_cbranch_scc1 .LBB0_144

.LBB0_147:
	s_ff1_i32_b64 s1, s[6:7]
	s_add_u32 s26, s6, -1
	s_addc_u32 s27, s7, -1
	s_lshl_b32 s24, s1, 10
	v_lshl_add_u64 v[16:17], v[2:3], 0, s[24:25]
	s_cmp_lg_u32 s1, s95
	s_cbranch_scc1 .Lsp_miss3
	s_waitcnt vmcnt(0)
	v_mov_b64_e32 v[20:21], v[82:83]
	v_mov_b64_e32 v[22:23], v[84:85]
	s_branch .Lsp_join3

.Lsp_join3:
	s_and_b64 s[6:7], s[26:27], s[6:7]
	s_waitcnt vmcnt(0)
	v_cvt_f64_f32_e32 v[16:17], v20
	v_cvt_f64_f32_e32 v[20:21], v21
	v_mul_f64 v[26:27], v[6:7], v[20:21]
	v_mul_f64 v[20:21], v[20:21], v[20:21]
	v_cvt_f64_f32_e32 v[24:25], v22
	v_fmac_f64_e32 v[26:27], v[4:5], v[16:17]
	v_fmac_f64_e32 v[20:21], v[16:17], v[16:17]
	v_cvt_f64_f32_e32 v[22:23], v23
	v_fmac_f64_e32 v[26:27], v[8:9], v[24:25]
	v_fmac_f64_e32 v[20:21], v[24:25], v[24:25]
	v_fmac_f64_e32 v[26:27], v[10:11], v[22:23]
	v_fmac_f64_e32 v[20:21], v[22:23], v[22:23]
	s_nop 0
	v_mov_b32_dpp v16, v26 quad_perm:[1,0,3,2] row_mask:0xf bank_mask:0xf bound_ctrl:1
	v_mov_b32_dpp v17, v27 quad_perm:[1,0,3,2] row_mask:0xf bank_mask:0xf bound_ctrl:1
	v_mov_b32_dpp v22, v20 quad_perm:[1,0,3,2] row_mask:0xf bank_mask:0xf bound_ctrl:1
	v_mov_b32_dpp v23, v21 quad_perm:[1,0,3,2] row_mask:0xf bank_mask:0xf bound_ctrl:1
	v_add_f64 v[16:17], v[26:27], v[16:17]
	v_add_f64 v[20:21], v[20:21], v[22:23]
	s_nop 0
	v_mov_b32_dpp v22, v16 quad_perm:[2,3,0,1] row_mask:0xf bank_mask:0xf bound_ctrl:1
	v_mov_b32_dpp v23, v17 quad_perm:[2,3,0,1] row_mask:0xf bank_mask:0xf bound_ctrl:1
	v_mov_b32_dpp v24, v20 quad_perm:[2,3,0,1] row_mask:0xf bank_mask:0xf bound_ctrl:1
	v_mov_b32_dpp v25, v21 quad_perm:[2,3,0,1] row_mask:0xf bank_mask:0xf bound_ctrl:1
	v_add_f64 v[16:17], v[16:17], v[22:23]
	v_add_f64 v[20:21], v[20:21], v[24:25]
	s_nop 0
	v_mov_b32_dpp v22, v16 row_half_mirror row_mask:0xf bank_mask:0xf bound_ctrl:1
	v_mov_b32_dpp v23, v17 row_half_mirror row_mask:0xf bank_mask:0xf bound_ctrl:1
	v_mov_b32_dpp v24, v20 row_half_mirror row_mask:0xf bank_mask:0xf bound_ctrl:1
	v_mov_b32_dpp v25, v21 row_half_mirror row_mask:0xf bank_mask:0xf bound_ctrl:1
	v_add_f64 v[16:17], v[16:17], v[22:23]
	v_add_f64 v[20:21], v[20:21], v[24:25]
	s_nop 0
	v_mov_b32_dpp v22, v16 row_mirror row_mask:0xf bank_mask:0xf bound_ctrl:1
	v_mov_b32_dpp v23, v17 row_mirror row_mask:0xf bank_mask:0xf bound_ctrl:1
	v_mov_b32_dpp v24, v20 row_mirror row_mask:0xf bank_mask:0xf bound_ctrl:1
	v_mov_b32_dpp v25, v21 row_mirror row_mask:0xf bank_mask:0xf bound_ctrl:1
	v_add_f64 v[16:17], v[16:17], v[22:23]
	v_add_f64 v[20:21], v[20:21], v[24:25]
	v_readlane_b32 s5, v17, 16
	v_readlane_b32 s9, v16, 16
	v_readlane_b32 s19, v17, 48
	v_readlane_b32 s23, v16, 48
	v_readlane_b32 s24, v21, 16
	v_readlane_b32 s33, v20, 16
	v_readlane_b32 s38, v21, 48
	v_readlane_b32 s39, v20, 48
	v_readlane_b32 s27, v17, 0
	v_readlane_b32 s26, v16, 0
	v_readlane_b32 s31, v17, 32
	v_readlane_b32 s30, v16, 32
	v_readlane_b32 s35, v21, 0
	v_readlane_b32 s34, v20, 0
	v_readlane_b32 s37, v21, 32
	v_readlane_b32 s36, v20, 32
	v_mov_b32_e32 v16, s9
	v_mov_b32_e32 v17, s5
	v_mov_b32_e32 v20, s23
	v_mov_b32_e32 v21, s19
	v_mov_b32_e32 v22, s33
	v_mov_b32_e32 v23, s24
	v_mov_b32_e32 v24, s39
	v_mov_b32_e32 v25, s38
	v_add_f64 v[16:17], s[26:27], v[16:17]
	v_add_f64 v[20:21], s[30:31], v[20:21]
	v_add_f64 v[22:23], s[34:35], v[22:23]
	v_add_f64 v[24:25], s[36:37], v[24:25]
	v_add_f64 v[16:17], v[16:17], v[20:21]
	v_add_f64 v[20:21], v[22:23], v[24:25]
	v_add_f64 v[20:21], v[12:13], v[20:21]
	v_fmac_f64_e32 v[20:21], -2.0, v[16:17]
	v_cvt_f32_f64_e32 v15, v[20:21]
	v_cmp_gt_f32_e32 vcc, v14, v15
	s_and_b64 s[26:27], vcc, exec
	s_cselect_b32 s4, s1, s4
	v_cndmask_b32_e32 v14, v14, v15, vcc
	s_cmp_lg_u64 s[6:7], 0
	s_cbranch_scc1 .LBB0_147
